# attention: unconditional bias reads (context chunks read an appended zero row), per-group branches and 240 dead zero-inits removed
# speedup vs baseline: 1.0023x; 1.0023x over previous
; __device__ __forceinline__ void ph_attn(const Frame& F, int j) {
;     ...
;         const int w0 = (F.wave & 3) * 16, myr0 = 4 * rp4 + 2 * (F.wave >> 2);
;         const int rlo = min(max(4 * rp4 - 4, 0), 120), rhi = min(max(4 * rp4 + 3 - 4, 0), 120) + 7;
;         const int nloc = lat ? (rhi - rlo + 1) : 0;
;         int qrow[2], r0t[2];
;         bf16x8 qf[2][2];
; #pragma unroll
;         for (int T = 0; T < 2; ++T) { r0t[T] = min(max(myr0 + T - 4, 0), 120);
;             qrow[T] = lat ? (TC + b * SEQ + (myr0 + T) * 64 + w0 + l15) : (b * CTXL + (2 * F.wave + T) * 16 + l15);
;             qf[T][0] = *(const bf16x8*)(P + (size_t)qrow[T] * 4096 + h * 64 + g * 8);
;             qf[T][1] = *(const bf16x8*)(P + (size_t)qrow[T] * 4096 + h * 64 + 32 + g * 8); }
;         if (lat) for (int i = F.tid; i < 480; i += 512) { const int rr = i >> 5, cc = i & 31; rp_l[i] = (cc < 31) ? rpb[h * 465 + rr * 31 + cc] * 1.4426950408889634f : -1e30f; }
;         f32x4 oacc[2][4];
; #pragma unroll
;         for (int T = 0; T < 2; ++T)
; #pragma unroll
;             for (int dt = 0; dt < 4; ++dt) oacc[T][dt] = (f32x4){0.f, 0.f, 0.f, 0.f};
;         float mrun[2] = {-1e30f, -1e30f}, lrun[2] = {0.f, 0.f};
;         const int nch = nloc + 4;
.LBB0_489:
	s_or_b64 exec, exec, s[4:5]
	s_lshl_b32 s4, s11, 7
	s_add_u32 s6, s82, s4
	s_addc_u32 s7, s83, 0
	v_lshlrev_b64 v[0:1], 13, v[126:127]
	v_lshl_add_u64 v[0:1], s[6:7], 0, v[0:1]
	v_lshl_add_u64 v[0:1], v[0:1], 0, v[118:119]
	global_load_dwordx4 v[4:7], v[0:1], off
	global_load_dwordx4 v[8:11], v[0:1], off offset:64
	v_lshlrev_b64 v[0:1], 13, v[124:125]
	v_lshl_add_u64 v[0:1], s[6:7], 0, v[0:1]
	v_lshl_add_u64 v[0:1], v[0:1], 0, v[118:119]
	global_load_dwordx4 v[12:15], v[0:1], off
	global_load_dwordx4 v[16:19], v[0:1], off offset:64
	s_mov_b64 s[6:7], exec
	s_andn2_b64 exec, exec, s[42:43]
	ds_write_b32 v197, v2
	s_mov_b64 exec, s[6:7]
	v_sub_u32_e64 v0, s2, 1 clamp
	s_lshl_b32 s4, s11, 6
	s_max_u32 s11, s2, 4
	v_min_u32_e32 v0, 0x78, v0
	v_subrev_u32_e32 v0, s11, v0
	v_add_u32_e32 v0, 12, v0
	v_cndmask_b32_e64 v214, 0, v0, s[46:47]
	v_sub_u32_e64 v0, s2, 4 clamp
	v_cmp_gt_i32_e32 vcc, 1, v214
	v_readfirstlane_b32 s13, v0
	v_add_u32_e32 v215, 3, v214
	s_cbranch_vccz .LBB0_491
	v_min_i32_e32 v0, 0, v215
	v_sub_u32_e32 v0, v0, v214
	v_lshlrev_b32_e32 v0, 6, v0
	v_add_u32_e32 v0, s9, v0
	s_cbranch_execz .LBB0_492
	s_branch .LBB0_493

.LBB0_514:
	v_mov_b64_e32 v[94:95], v[74:75]
	v_mov_b64_e32 v[98:99], v[82:83]
	v_mov_b64_e32 v[106:107], v[86:87]
	v_mov_b64_e32 v[114:115], v[102:103]
	s_andn2_b64 vcc, exec, s[0:1]
	v_mov_b32_e32 v132, v218
	v_mov_b64_e32 v[92:93], v[72:73]
	v_mov_b64_e32 v[96:97], v[80:81]
	v_mov_b64_e32 v[104:105], v[84:85]
	v_mov_b64_e32 v[112:113], v[100:101]
	s_cbranch_vccnz .LBB0_524
	s_add_i32 s2, s29, 0xffffffa0
	s_and_b64 s[0:1], s[46:47], exec
	s_cselect_b32 s0, 0x1e0, s2
	s_lshl_b32 s0, s0, 2
	v_cndmask_b32_e64 v3, 0, 1, s[48:49]
	s_add_i32 s0, s0, 0
	v_cmp_ne_u32_e64 s[50:51], 1, v3
	s_andn2_b64 vcc, exec, s[48:49]
	v_lshl_add_u32 v3, v159, 2, s0
	v_lshl_add_u32 v29, v160, 2, s0
	v_lshl_add_u32 v30, v161, 2, s0
	v_lshl_add_u32 v31, v162, 2, s0
	ds_read_b32 v32, v3 offset:36864
	ds_read_b32 v33, v29 offset:36864
	ds_read_b32 v34, v30 offset:36864
	ds_read_b32 v35, v31 offset:36864
.LBB0_517:
	s_and_b64 vcc, exec, s[50:51]
	v_lshl_add_u32 v3, v163, 2, s0
	v_lshl_add_u32 v29, v164, 2, s0
	v_lshl_add_u32 v30, v165, 2, s0
	v_lshl_add_u32 v31, v166, 2, s0
	ds_read_b32 v28, v3 offset:36864
	ds_read_b32 v29, v29 offset:36864
	ds_read_b32 v30, v30 offset:36864
	ds_read_b32 v31, v31 offset:36864
.LBB0_519:
	s_and_b64 vcc, exec, s[50:51]
	v_lshl_add_u32 v3, v167, 2, s0
	v_lshl_add_u32 v69, v168, 2, s0
	v_lshl_add_u32 v70, v169, 2, s0
	v_lshl_add_u32 v71, v170, 2, s0
	ds_read_b32 v76, v3 offset:36864
	ds_read_b32 v77, v69 offset:36864
	ds_read_b32 v78, v70 offset:36864
	ds_read_b32 v79, v71 offset:36864
.LBB0_521:
	s_and_b64 vcc, exec, s[50:51]
	v_lshl_add_u32 v3, v171, 2, s0
	v_lshl_add_u32 v69, v172, 2, s0
	v_lshl_add_u32 v70, v173, 2, s0
	v_lshl_add_u32 v71, v190, 2, s0
	ds_read_b32 v68, v3 offset:36864
	ds_read_b32 v69, v69 offset:36864
	ds_read_b32 v70, v70 offset:36864
	ds_read_b32 v71, v71 offset:36864

.LBB0_525:
	s_andn2_b64 vcc, exec, s[0:1]
	s_cbranch_vccnz .LBB0_543
	s_add_i32 s2, s29, 0xffffffa0
	s_and_b64 s[0:1], s[46:47], exec
	s_cselect_b32 s0, 0x1e0, s2
	s_lshl_b32 s0, s0, 2
	v_cndmask_b32_e64 v3, 0, 1, s[48:49]
	s_add_i32 s0, s0, 0
	v_cmp_ne_u32_e64 s[50:51], 1, v3
	s_andn2_b64 vcc, exec, s[48:49]
	v_lshl_add_u32 v3, v159, 2, s0
	v_lshl_add_u32 v29, v160, 2, s0
	v_lshl_add_u32 v30, v161, 2, s0
	v_lshl_add_u32 v31, v162, 2, s0
	ds_read_b32 v68, v3 offset:36864
	ds_read_b32 v69, v29 offset:36864
	ds_read_b32 v70, v30 offset:36864
	ds_read_b32 v71, v31 offset:36864

.LBB0_530:
	s_and_b64 vcc, exec, s[50:51]
	v_lshl_add_u32 v3, v167, 2, s0
	v_lshl_add_u32 v33, v168, 2, s0
	v_lshl_add_u32 v34, v169, 2, s0
	v_lshl_add_u32 v35, v170, 2, s0
	ds_read_b32 v92, v3 offset:36864
	ds_read_b32 v93, v33 offset:36864
	ds_read_b32 v94, v34 offset:36864
	ds_read_b32 v95, v35 offset:36864
.LBB0_532:
	s_and_b64 vcc, exec, s[50:51]
	v_lshl_add_u32 v3, v171, 2, s0
	v_lshl_add_u32 v33, v172, 2, s0
	v_lshl_add_u32 v34, v173, 2, s0
	v_lshl_add_u32 v35, v190, 2, s0
	ds_read_b32 v32, v3 offset:36864
	ds_read_b32 v33, v33 offset:36864
	ds_read_b32 v34, v34 offset:36864
	ds_read_b32 v35, v35 offset:36864
.LBB0_534:
	s_add_i32 s2, s29, 0xffffff80
	s_and_b64 s[0:1], s[46:47], exec
	s_cselect_b32 s0, 0x1e0, s2
	s_lshl_b32 s0, s0, 2
	s_add_i32 s0, s0, 0
	s_and_b64 vcc, exec, s[50:51]
	v_lshl_add_u32 v3, v159, 2, s0
	v_lshl_add_u32 v77, v160, 2, s0
	v_lshl_add_u32 v78, v161, 2, s0
	v_lshl_add_u32 v79, v162, 2, s0
	ds_read_b32 v76, v3 offset:36864
	ds_read_b32 v77, v77 offset:36864
	ds_read_b32 v78, v78 offset:36864
	ds_read_b32 v79, v79 offset:36864
.LBB0_536:
	s_and_b64 vcc, exec, s[50:51]
	v_lshl_add_u32 v3, v163, 2, s0
	v_lshl_add_u32 v89, v164, 2, s0
	v_lshl_add_u32 v90, v165, 2, s0
	v_lshl_add_u32 v91, v166, 2, s0
	ds_read_b32 v88, v3 offset:36864
	ds_read_b32 v89, v89 offset:36864
	ds_read_b32 v90, v90 offset:36864
	ds_read_b32 v91, v91 offset:36864
.LBB0_538:
	s_and_b64 vcc, exec, s[50:51]
	v_lshl_add_u32 v3, v167, 2, s0
	v_lshl_add_u32 v97, v168, 2, s0
	v_lshl_add_u32 v98, v169, 2, s0
	v_lshl_add_u32 v99, v170, 2, s0
	ds_read_b32 v104, v3 offset:36864
	ds_read_b32 v105, v97 offset:36864
	ds_read_b32 v106, v98 offset:36864
	ds_read_b32 v107, v99 offset:36864
.LBB0_540:
	s_and_b64 vcc, exec, s[50:51]
	v_lshl_add_u32 v3, v171, 2, s0
	v_lshl_add_u32 v97, v172, 2, s0
	v_lshl_add_u32 v98, v173, 2, s0
	v_lshl_add_u32 v99, v190, 2, s0
	ds_read_b32 v96, v3 offset:36864
	ds_read_b32 v97, v97 offset:36864
	ds_read_b32 v98, v98 offset:36864
	ds_read_b32 v99, v99 offset:36864

; #define LAS __attribute__((address_space(3)))
; #define ATT_WRITE(buf_, kq_, vq_) do { const int key = F.tid >> 3, ds = (F.tid & 7) * 8; LAS bf16_t* Kd = Ks0 + (buf_) * 9216; LAS bf16_t* Vd = Kd + 4608; \
;             *(LAS u32x4*)(Kd + key * 72 + ds) = kq_; *(LAS u32x4*)(Vd + key * 72 + ds) = vq_; } while (0)
; __device__ __forceinline__ void ph_attn(const Frame& F, int j) {
;     ...
;         auto chunk = [&](const int ch, u32x4& kw, u32x4& vw, u32x4& kl, u32x4& vl) __attribute__((always_inline)) {
;             const bool loc = ch < nloc; const int kr = rlo + ch;
;             ATT_WRITE((ch + 1) & 1, kw, vw);
;             ATT_LOAD(kl, vl, ch + 4);
;             const LAS bf16_t* Ks = Ks0 + (ch & 1) * 9216; const LAS bf16_t* Vt = Ks + 4608;
;             const bool m0 = (ch < nch) && (loc ? (kr >= r0t[0] && kr < r0t[0] + 8) : true);
;             const bool m1 = (ch < nch) && (loc ? (kr >= r0t[1] && kr < r0t[1] + 8) : true);
;             if (m0 && m1) ATT_COMPUTE(3); else if (m0) ATT_COMPUTE(1); else if (m1) ATT_COMPUTE(2);
.LBB0_543:
	s_add_i32 s0, s30, -2
	v_mov_b32_e32 v28, s13
	v_cmp_lt_i32_e32 vcc, s0, v214
	v_min_i32_e32 v3, s0, v215
	v_mov_b32_e32 v29, s9
	v_cndmask_b32_e32 v28, v216, v28, vcc
	v_mov_b32_e32 v30, s26
	v_add_u32_e32 v3, v28, v3
	v_cndmask_b32_e32 v29, v29, v30, vcc
	v_lshlrev_b32_e32 v3, 6, v3
	v_add_u32_e32 v3, v3, v29
	v_add_u32_e32 v28, v3, v194
	v_ashrrev_i32_e32 v29, 31, v28
	v_lshlrev_b64 v[28:29], 13, v[28:29]
	s_waitcnt lgkmcnt(0)
	s_barrier
	v_lshl_add_u64 v[32:33], v[0:1], 0, v[28:29]
	global_load_dwordx4 v[28:31], v[32:33], off offset:1024
	s_nop 0
	global_load_dwordx4 v[32:35], v[32:33], off offset:2048
	s_add_i32 s2, s30, -6
	s_add_i32 s6, s54, -10
	s_cmp_ge_u32 s6, s24
	s_cselect_b64 s[0:1], -1, 0
	s_cmp_lt_u32 s6, s27
	s_cselect_b64 s[4:5], -1, 0
	s_and_b64 s[0:1], s[0:1], s[4:5]
	s_cmp_ge_u32 s6, s25
	s_cselect_b64 s[4:5], -1, 0
	s_cmp_lt_u32 s6, s28
	s_cselect_b64 s[6:7], -1, 0
	v_cmp_lt_i32_e32 vcc, s2, v121
	s_waitcnt vmcnt(7)
	ds_write_b128 v196, v[20:23]
	s_waitcnt vmcnt(6)
	ds_write_b128 v196, v[24:27] offset:9216
	v_cndmask_b32_e64 v3, 0, 1, s[0:1]
	v_cndmask_b32_e64 v20, 0, 1, vcc
	v_cmp_lt_i32_e64 s[48:49], s2, v214
	s_and_b64 s[0:1], s[4:5], s[6:7]
	v_cndmask_b32_e64 v21, 0, 1, s[0:1]
	v_cndmask_b32_e64 v3, v20, v3, s[48:49]
	v_cndmask_b32_e64 v20, v20, v21, s[48:49]
	v_and_b32_e32 v3, 1, v3
	v_cmp_eq_u32_e64 s[52:53], 1, v3
	v_and_b32_e32 v3, 1, v20
	v_cmp_eq_u32_e64 s[50:51], 1, v3
	s_and_b64 s[0:1], s[52:53], s[50:51]
	s_andn2_b64 vcc, exec, s[0:1]
	s_mov_b64 s[0:1], -1
	s_cbranch_vccz .LBB0_567
	s_xor_b64 s[4:5], s[52:53], -1
	s_and_b64 vcc, exec, s[4:5]
	s_cbranch_vccz .LBB0_556
	v_mov_b64_e32 v[52:53], v[68:69]
	v_mov_b64_e32 v[56:57], v[76:77]
	v_mov_b64_e32 v[60:61], v[88:89]
	v_mov_b64_e32 v[84:85], v[108:109]
	s_andn2_b64 vcc, exec, s[50:51]
	v_mov_b64_e32 v[128:129], v[130:131]
	v_mov_b32_e32 v3, v134
	v_mov_b64_e32 v[54:55], v[70:71]
	v_mov_b64_e32 v[58:59], v[78:79]
	v_mov_b64_e32 v[62:63], v[90:91]
	v_mov_b64_e32 v[86:87], v[110:111]
	s_cbranch_vccnz .LBB0_555
	s_add_i32 s2, s29, 0xffffffa0
	s_and_b64 s[0:1], s[48:49], exec
	s_cselect_b32 s0, s2, 0x1e0
	s_lshl_b32 s0, s0, 2
	v_cndmask_b32_e64 v3, 0, 1, s[48:49]
	s_add_i32 s0, s0, 0
	v_cmp_ne_u32_e64 s[50:51], 1, v3
	s_andn2_b64 vcc, exec, s[48:49]
	v_lshl_add_u32 v3, v159, 2, s0
	v_lshl_add_u32 v21, v160, 2, s0
	v_lshl_add_u32 v22, v161, 2, s0
	v_lshl_add_u32 v23, v162, 2, s0
	ds_read_b32 v24, v3 offset:36864
	ds_read_b32 v25, v21 offset:36864
	ds_read_b32 v26, v22 offset:36864
	ds_read_b32 v27, v23 offset:36864
.LBB0_548:
	s_and_b64 vcc, exec, s[50:51]
	v_lshl_add_u32 v3, v163, 2, s0
	v_lshl_add_u32 v21, v164, 2, s0
	v_lshl_add_u32 v22, v165, 2, s0
	v_lshl_add_u32 v23, v166, 2, s0
	ds_read_b32 v20, v3 offset:36864
	ds_read_b32 v21, v21 offset:36864
	ds_read_b32 v22, v22 offset:36864
	ds_read_b32 v23, v23 offset:36864
.LBB0_550:
	s_and_b64 vcc, exec, s[50:51]
	v_lshl_add_u32 v3, v167, 2, s0
	v_lshl_add_u32 v53, v168, 2, s0
	v_lshl_add_u32 v54, v169, 2, s0
	v_lshl_add_u32 v55, v170, 2, s0
	ds_read_b32 v56, v3 offset:36864
	ds_read_b32 v57, v53 offset:36864
	ds_read_b32 v58, v54 offset:36864
	ds_read_b32 v59, v55 offset:36864
.LBB0_552:
	s_and_b64 vcc, exec, s[50:51]
	v_lshl_add_u32 v3, v171, 2, s0
	v_lshl_add_u32 v53, v172, 2, s0
	v_lshl_add_u32 v54, v173, 2, s0
	v_lshl_add_u32 v55, v190, 2, s0
	ds_read_b32 v52, v3 offset:36864
	ds_read_b32 v53, v53 offset:36864
	ds_read_b32 v54, v54 offset:36864
	ds_read_b32 v55, v55 offset:36864

.LBB0_556:
	v_mov_b64_e32 v[64:65], v[92:93]
	v_mov_b64_e32 v[72:73], v[96:97]
	v_mov_b64_e32 v[80:81], v[104:105]
	v_mov_b64_e32 v[100:101], v[112:113]
	s_andn2_b64 vcc, exec, s[0:1]
	v_mov_b32_e32 v217, v132
	v_mov_b64_e32 v[66:67], v[94:95]
	v_mov_b64_e32 v[74:75], v[98:99]
	v_mov_b64_e32 v[82:83], v[106:107]
	v_mov_b64_e32 v[102:103], v[114:115]
	s_cbranch_vccnz .LBB0_566
	s_sub_i32 s2, s29, 64
	s_and_b64 s[0:1], s[48:49], exec
	s_cselect_b32 s0, s2, 0x1e0
	s_lshl_b32 s0, s0, 2
	v_cndmask_b32_e64 v3, 0, 1, s[48:49]
	s_add_i32 s0, s0, 0
	v_cmp_ne_u32_e64 s[50:51], 1, v3
	s_andn2_b64 vcc, exec, s[48:49]
	v_lshl_add_u32 v3, v159, 2, s0
	v_lshl_add_u32 v21, v160, 2, s0
	v_lshl_add_u32 v22, v161, 2, s0
	v_lshl_add_u32 v23, v162, 2, s0
	ds_read_b32 v24, v3 offset:36864
	ds_read_b32 v25, v21 offset:36864
	ds_read_b32 v26, v22 offset:36864
	ds_read_b32 v27, v23 offset:36864

.LBB0_567:
	s_andn2_b64 vcc, exec, s[0:1]
	s_cbranch_vccnz .LBB0_585
	s_sub_i32 s2, s29, 64
	s_and_b64 s[0:1], s[48:49], exec
	s_cselect_b32 s0, s2, 0x1e0
	s_lshl_b32 s0, s0, 2
	v_cndmask_b32_e64 v3, 0, 1, s[48:49]
	s_add_i32 s0, s0, 0
	v_cmp_ne_u32_e64 s[50:51], 1, v3
	s_andn2_b64 vcc, exec, s[48:49]
	v_lshl_add_u32 v3, v159, 2, s0
	v_lshl_add_u32 v21, v160, 2, s0
	v_lshl_add_u32 v22, v161, 2, s0
	v_lshl_add_u32 v23, v162, 2, s0
	ds_read_b32 v52, v3 offset:36864
	ds_read_b32 v53, v21 offset:36864
	ds_read_b32 v54, v22 offset:36864
	ds_read_b32 v55, v23 offset:36864

.LBB0_572:
	s_and_b64 vcc, exec, s[50:51]
	v_lshl_add_u32 v3, v167, 2, s0
	v_lshl_add_u32 v25, v168, 2, s0
	v_lshl_add_u32 v26, v169, 2, s0
	v_lshl_add_u32 v27, v170, 2, s0
	ds_read_b32 v56, v3 offset:36864
	ds_read_b32 v57, v25 offset:36864
	ds_read_b32 v58, v26 offset:36864
	ds_read_b32 v59, v27 offset:36864
.LBB0_574:
	s_and_b64 vcc, exec, s[50:51]
	v_lshl_add_u32 v3, v171, 2, s0
	v_lshl_add_u32 v25, v172, 2, s0
	v_lshl_add_u32 v26, v173, 2, s0
	v_lshl_add_u32 v27, v190, 2, s0
	ds_read_b32 v24, v3 offset:36864
	ds_read_b32 v25, v25 offset:36864
	ds_read_b32 v26, v26 offset:36864
	ds_read_b32 v27, v27 offset:36864
.LBB0_576:
	s_add_i32 s2, s29, 0xffffffa0
	s_and_b64 s[0:1], s[48:49], exec
	s_cselect_b32 s0, s2, 0x1e0
	s_lshl_b32 s0, s0, 2
	s_add_i32 s0, s0, 0
	s_and_b64 vcc, exec, s[50:51]
	v_lshl_add_u32 v3, v159, 2, s0
	v_lshl_add_u32 v61, v160, 2, s0
	v_lshl_add_u32 v62, v161, 2, s0
	v_lshl_add_u32 v63, v162, 2, s0
	ds_read_b32 v60, v3 offset:36864
	ds_read_b32 v61, v61 offset:36864
	ds_read_b32 v62, v62 offset:36864
	ds_read_b32 v63, v63 offset:36864
.LBB0_578:
	s_and_b64 vcc, exec, s[50:51]
	v_lshl_add_u32 v3, v163, 2, s0
	v_lshl_add_u32 v65, v164, 2, s0
	v_lshl_add_u32 v66, v165, 2, s0
	v_lshl_add_u32 v67, v166, 2, s0
	ds_read_b32 v64, v3 offset:36864
	ds_read_b32 v65, v65 offset:36864
	ds_read_b32 v66, v66 offset:36864
	ds_read_b32 v67, v67 offset:36864
.LBB0_580:
	s_and_b64 vcc, exec, s[50:51]
	v_lshl_add_u32 v3, v167, 2, s0
	v_lshl_add_u32 v73, v168, 2, s0
	v_lshl_add_u32 v74, v169, 2, s0
	v_lshl_add_u32 v75, v170, 2, s0
	ds_read_b32 v100, v3 offset:36864
	ds_read_b32 v101, v73 offset:36864
	ds_read_b32 v102, v74 offset:36864
	ds_read_b32 v103, v75 offset:36864
.LBB0_582:
	s_and_b64 vcc, exec, s[50:51]
	v_lshl_add_u32 v3, v171, 2, s0
	v_lshl_add_u32 v73, v172, 2, s0
	v_lshl_add_u32 v74, v173, 2, s0
	v_lshl_add_u32 v75, v190, 2, s0
	ds_read_b32 v72, v3 offset:36864
	ds_read_b32 v73, v73 offset:36864
	ds_read_b32 v74, v74 offset:36864
	ds_read_b32 v75, v75 offset:36864

; #define LAS __attribute__((address_space(3)))
; #define ATT_WRITE(buf_, kq_, vq_) do { const int key = F.tid >> 3, ds = (F.tid & 7) * 8; LAS bf16_t* Kd = Ks0 + (buf_) * 9216; LAS bf16_t* Vd = Kd + 4608; \
;             *(LAS u32x4*)(Kd + key * 72 + ds) = kq_; *(LAS u32x4*)(Vd + key * 72 + ds) = vq_; } while (0)
; __device__ __forceinline__ void ph_attn(const Frame& F, int j) {
;     ...
;         auto chunk = [&](const int ch, u32x4& kw, u32x4& vw, u32x4& kl, u32x4& vl) __attribute__((always_inline)) {
;             const bool loc = ch < nloc; const int kr = rlo + ch;
;             ATT_WRITE((ch + 1) & 1, kw, vw);
;             ATT_LOAD(kl, vl, ch + 4);
;             const LAS bf16_t* Ks = Ks0 + (ch & 1) * 9216; const LAS bf16_t* Vt = Ks + 4608;
;             const bool m0 = (ch < nch) && (loc ? (kr >= r0t[0] && kr < r0t[0] + 8) : true);
;             const bool m1 = (ch < nch) && (loc ? (kr >= r0t[1] && kr < r0t[1] + 8) : true);
;             if (m0 && m1) ATT_COMPUTE(3); else if (m0) ATT_COMPUTE(1); else if (m1) ATT_COMPUTE(2);
.LBB0_585:
	s_add_i32 s0, s30, -1
	v_mov_b32_e32 v21, s13
	v_cmp_lt_i32_e32 vcc, s0, v214
	v_min_i32_e32 v20, s0, v215
	v_mov_b32_e32 v22, s9
	v_cndmask_b32_e32 v21, v216, v21, vcc
	v_mov_b32_e32 v23, s26
	v_add_u32_e32 v20, v21, v20
	v_cndmask_b32_e32 v22, v22, v23, vcc
	v_lshlrev_b32_e32 v20, 6, v20
	v_add_u32_e32 v20, v20, v22
	v_add_u32_e32 v20, v20, v194
	v_ashrrev_i32_e32 v21, 31, v20
	v_lshlrev_b64 v[20:21], 13, v[20:21]
	s_waitcnt lgkmcnt(0)
	s_barrier
	v_lshl_add_u64 v[24:25], v[0:1], 0, v[20:21]
	global_load_dwordx4 v[20:23], v[24:25], off offset:1024
	s_nop 0
	global_load_dwordx4 v[24:27], v[24:25], off offset:2048
	s_add_i32 s2, s30, -5
	s_add_i32 s6, s54, -9
	s_cmp_ge_u32 s6, s24
	s_cselect_b64 s[0:1], -1, 0
	s_cmp_lt_u32 s6, s27
	s_cselect_b64 s[4:5], -1, 0
	s_and_b64 s[0:1], s[0:1], s[4:5]
	s_cmp_ge_u32 s6, s25
	s_cselect_b64 s[4:5], -1, 0
	s_cmp_lt_u32 s6, s28
	s_cselect_b64 s[6:7], -1, 0
	v_cmp_lt_i32_e32 vcc, s2, v121
	s_waitcnt vmcnt(7)
	ds_write_b128 v196, v[36:39] offset:18432
	s_waitcnt vmcnt(6)
	ds_write_b128 v196, v[40:43] offset:27648
	v_cndmask_b32_e64 v36, 0, 1, s[0:1]
	v_cndmask_b32_e64 v37, 0, 1, vcc
	v_cmp_lt_i32_e64 s[48:49], s2, v214
	s_and_b64 s[0:1], s[4:5], s[6:7]
	v_cndmask_b32_e64 v38, 0, 1, s[0:1]
	v_cndmask_b32_e64 v36, v37, v36, s[48:49]
	v_cndmask_b32_e64 v37, v37, v38, s[48:49]
	v_and_b32_e32 v36, 1, v36
	v_cmp_eq_u32_e64 s[52:53], 1, v36
	v_and_b32_e32 v36, 1, v37
	v_cmp_eq_u32_e64 s[50:51], 1, v36
	s_and_b64 s[0:1], s[52:53], s[50:51]
	s_andn2_b64 vcc, exec, s[0:1]
	s_mov_b64 s[0:1], -1
	s_cbranch_vccz .LBB0_609
	s_xor_b64 s[4:5], s[52:53], -1
	s_and_b64 vcc, exec, s[4:5]
	s_cbranch_vccz .LBB0_598
	v_mov_b64_e32 v[70:71], v[54:55]
	v_mov_b64_e32 v[78:79], v[58:59]
	v_mov_b64_e32 v[90:91], v[62:63]
	v_mov_b64_e32 v[110:111], v[86:87]
	s_andn2_b64 vcc, exec, s[50:51]
	v_mov_b64_e32 v[130:131], v[128:129]
	v_mov_b32_e32 v219, v3
	v_mov_b64_e32 v[68:69], v[52:53]
	v_mov_b64_e32 v[76:77], v[56:57]
	v_mov_b64_e32 v[88:89], v[60:61]
	v_mov_b64_e32 v[108:109], v[84:85]
	s_cbranch_vccnz .LBB0_597
	s_sub_i32 s2, s29, 64
	s_and_b64 s[0:1], s[48:49], exec
	s_cselect_b32 s0, s2, 0x1e0
	s_lshl_b32 s0, s0, 2
	v_cndmask_b32_e64 v37, 0, 1, s[48:49]
	s_add_i32 s0, s0, 0
	v_cmp_ne_u32_e64 s[50:51], 1, v37
	s_andn2_b64 vcc, exec, s[48:49]
	v_lshl_add_u32 v37, v159, 2, s0
	v_lshl_add_u32 v43, v162, 2, s0
	v_lshl_add_u32 v38, v160, 2, s0
	v_lshl_add_u32 v39, v161, 2, s0
	ds_read_b32 v40, v37 offset:36864
	ds_read_b32 v41, v38 offset:36864
	ds_read_b32 v42, v39 offset:36864
	ds_read_b32 v43, v43 offset:36864
.LBB0_590:
	s_and_b64 vcc, exec, s[50:51]
	v_lshl_add_u32 v36, v163, 2, s0
	v_lshl_add_u32 v37, v164, 2, s0
	v_lshl_add_u32 v38, v165, 2, s0
	v_lshl_add_u32 v39, v166, 2, s0
	ds_read_b32 v36, v36 offset:36864
	ds_read_b32 v37, v37 offset:36864
	ds_read_b32 v38, v38 offset:36864
	ds_read_b32 v39, v39 offset:36864
.LBB0_592:
	s_and_b64 vcc, exec, s[50:51]
	v_lshl_add_u32 v69, v167, 2, s0
	v_lshl_add_u32 v79, v170, 2, s0
	v_lshl_add_u32 v70, v168, 2, s0
	v_lshl_add_u32 v71, v169, 2, s0
	ds_read_b32 v76, v69 offset:36864
	ds_read_b32 v77, v70 offset:36864
	ds_read_b32 v78, v71 offset:36864
	ds_read_b32 v79, v79 offset:36864
.LBB0_594:
	s_and_b64 vcc, exec, s[50:51]
	v_lshl_add_u32 v68, v171, 2, s0
	v_lshl_add_u32 v69, v172, 2, s0
	v_lshl_add_u32 v70, v173, 2, s0
	v_lshl_add_u32 v71, v190, 2, s0
	ds_read_b32 v68, v68 offset:36864
	ds_read_b32 v69, v69 offset:36864
	ds_read_b32 v70, v70 offset:36864
	ds_read_b32 v71, v71 offset:36864

.LBB0_598:
	v_mov_b64_e32 v[94:95], v[66:67]
	v_mov_b64_e32 v[98:99], v[74:75]
	v_mov_b64_e32 v[106:107], v[82:83]
	v_mov_b64_e32 v[114:115], v[102:103]
	s_andn2_b64 vcc, exec, s[0:1]
	v_mov_b32_e32 v220, v217
	v_mov_b64_e32 v[92:93], v[64:65]
	v_mov_b64_e32 v[96:97], v[72:73]
	v_mov_b64_e32 v[104:105], v[80:81]
	v_mov_b64_e32 v[112:113], v[100:101]
	s_cbranch_vccnz .LBB0_608
	s_sub_i32 s2, s29, 32
	s_and_b64 s[0:1], s[48:49], exec
	s_cselect_b32 s0, s2, 0x1e0
	s_lshl_b32 s0, s0, 2
	v_cndmask_b32_e64 v37, 0, 1, s[48:49]
	s_add_i32 s0, s0, 0
	v_cmp_ne_u32_e64 s[50:51], 1, v37
	s_andn2_b64 vcc, exec, s[48:49]
	v_lshl_add_u32 v37, v159, 2, s0
	v_lshl_add_u32 v43, v162, 2, s0
	v_lshl_add_u32 v38, v160, 2, s0
	v_lshl_add_u32 v39, v161, 2, s0
	ds_read_b32 v40, v37 offset:36864
	ds_read_b32 v41, v38 offset:36864
	ds_read_b32 v42, v39 offset:36864
	ds_read_b32 v43, v43 offset:36864

.LBB0_609:
	s_andn2_b64 vcc, exec, s[0:1]
	s_cbranch_vccnz .LBB0_627
	s_sub_i32 s2, s29, 32
	s_and_b64 s[0:1], s[48:49], exec
	s_cselect_b32 s0, s2, 0x1e0
	s_lshl_b32 s0, s0, 2
	v_cndmask_b32_e64 v37, 0, 1, s[48:49]
	s_add_i32 s0, s0, 0
	v_cmp_ne_u32_e64 s[50:51], 1, v37
	s_andn2_b64 vcc, exec, s[48:49]
	v_lshl_add_u32 v37, v159, 2, s0
	v_lshl_add_u32 v38, v160, 2, s0
	v_lshl_add_u32 v39, v161, 2, s0
	v_lshl_add_u32 v40, v162, 2, s0
	ds_read_b32 v68, v37 offset:36864
	ds_read_b32 v69, v38 offset:36864
	ds_read_b32 v70, v39 offset:36864
	ds_read_b32 v71, v40 offset:36864

.LBB0_614:
	s_and_b64 vcc, exec, s[50:51]
	v_lshl_add_u32 v41, v167, 2, s0
	v_lshl_add_u32 v79, v170, 2, s0
	v_lshl_add_u32 v42, v168, 2, s0
	v_lshl_add_u32 v43, v169, 2, s0
	ds_read_b32 v76, v41 offset:36864
	ds_read_b32 v77, v42 offset:36864
	ds_read_b32 v78, v43 offset:36864
	ds_read_b32 v79, v79 offset:36864
.LBB0_616:
	s_and_b64 vcc, exec, s[50:51]
	v_lshl_add_u32 v40, v171, 2, s0
	v_lshl_add_u32 v41, v172, 2, s0
	v_lshl_add_u32 v42, v173, 2, s0
	v_lshl_add_u32 v43, v190, 2, s0
	ds_read_b32 v40, v40 offset:36864
	ds_read_b32 v41, v41 offset:36864
	ds_read_b32 v42, v42 offset:36864
	ds_read_b32 v43, v43 offset:36864
.LBB0_618:
	s_sub_i32 s2, s29, 64
	s_and_b64 s[0:1], s[48:49], exec
	s_cselect_b32 s0, s2, 0x1e0
	s_lshl_b32 s0, s0, 2
	s_add_i32 s0, s0, 0
	s_and_b64 vcc, exec, s[50:51]
	v_lshl_add_u32 v89, v159, 2, s0
	v_lshl_add_u32 v95, v162, 2, s0
	v_lshl_add_u32 v90, v160, 2, s0
	v_lshl_add_u32 v91, v161, 2, s0
	ds_read_b32 v92, v89 offset:36864
	ds_read_b32 v93, v90 offset:36864
	ds_read_b32 v94, v91 offset:36864
	ds_read_b32 v95, v95 offset:36864
.LBB0_620:
	s_and_b64 vcc, exec, s[50:51]
	v_lshl_add_u32 v88, v163, 2, s0
	v_lshl_add_u32 v89, v164, 2, s0
	v_lshl_add_u32 v90, v165, 2, s0
	v_lshl_add_u32 v91, v166, 2, s0
	ds_read_b32 v88, v88 offset:36864
	ds_read_b32 v89, v89 offset:36864
	ds_read_b32 v90, v90 offset:36864
	ds_read_b32 v91, v91 offset:36864
.LBB0_622:
	s_and_b64 vcc, exec, s[50:51]
	v_lshl_add_u32 v96, v167, 2, s0
	v_lshl_add_u32 v97, v168, 2, s0
	v_lshl_add_u32 v98, v169, 2, s0
	v_lshl_add_u32 v99, v170, 2, s0
	ds_read_b32 v96, v96 offset:36864
	ds_read_b32 v97, v97 offset:36864
	ds_read_b32 v98, v98 offset:36864
	ds_read_b32 v99, v99 offset:36864
.LBB0_624:
	s_and_b64 vcc, exec, s[50:51]
	v_lshl_add_u32 v104, v171, 2, s0
	v_lshl_add_u32 v105, v172, 2, s0
	v_lshl_add_u32 v106, v173, 2, s0
	v_lshl_add_u32 v107, v190, 2, s0
	ds_read_b32 v104, v104 offset:36864
	ds_read_b32 v105, v105 offset:36864
	ds_read_b32 v106, v106 offset:36864
	ds_read_b32 v107, v107 offset:36864

; #define LAS __attribute__((address_space(3)))
; #define ATT_WRITE(buf_, kq_, vq_) do { const int key = F.tid >> 3, ds = (F.tid & 7) * 8; LAS bf16_t* Kd = Ks0 + (buf_) * 9216; LAS bf16_t* Vd = Kd + 4608; \
;             *(LAS u32x4*)(Kd + key * 72 + ds) = kq_; *(LAS u32x4*)(Vd + key * 72 + ds) = vq_; } while (0)
; __device__ __forceinline__ void ph_attn(const Frame& F, int j) {
;     ...
;         auto chunk = [&](const int ch, u32x4& kw, u32x4& vw, u32x4& kl, u32x4& vl) __attribute__((always_inline)) {
;             const bool loc = ch < nloc; const int kr = rlo + ch;
;             ATT_WRITE((ch + 1) & 1, kw, vw);
;             ATT_LOAD(kl, vl, ch + 4);
;             const LAS bf16_t* Ks = Ks0 + (ch & 1) * 9216; const LAS bf16_t* Vt = Ks + 4608;
;             const bool m0 = (ch < nch) && (loc ? (kr >= r0t[0] && kr < r0t[0] + 8) : true);
;             const bool m1 = (ch < nch) && (loc ? (kr >= r0t[1] && kr < r0t[1] + 8) : true);
;             if (m0 && m1) ATT_COMPUTE(3); else if (m0) ATT_COMPUTE(1); else if (m1) ATT_COMPUTE(2);
.LBB0_627:
	v_mov_b32_e32 v36, s13
	v_cmp_lt_i32_e32 vcc, s30, v214
	v_min_i32_e32 v3, s30, v215
	v_mov_b32_e32 v37, s9
	v_cndmask_b32_e32 v36, v216, v36, vcc
	v_mov_b32_e32 v38, s26
	v_add_u32_e32 v3, v36, v3
	v_cndmask_b32_e32 v37, v37, v38, vcc
	v_lshlrev_b32_e32 v3, 6, v3
	v_add_u32_e32 v3, v3, v37
	v_add_u32_e32 v36, v3, v194
	v_ashrrev_i32_e32 v37, 31, v36
	v_lshlrev_b64 v[36:37], 13, v[36:37]
	s_waitcnt lgkmcnt(0)
	s_barrier
	v_lshl_add_u64 v[40:41], v[0:1], 0, v[36:37]
	global_load_dwordx4 v[36:39], v[40:41], off offset:1024
	s_nop 0
	global_load_dwordx4 v[40:43], v[40:41], off offset:2048
	s_add_i32 s2, s30, -4
	s_add_i32 s54, s54, -8
	s_cmp_ge_u32 s54, s24
	s_cselect_b64 s[0:1], -1, 0
	s_cmp_lt_u32 s54, s27
	s_cselect_b64 s[4:5], -1, 0
	s_and_b64 s[0:1], s[0:1], s[4:5]
	s_cmp_ge_u32 s54, s25
	s_cselect_b64 s[4:5], -1, 0
	s_cmp_lt_u32 s54, s28
	s_cselect_b64 s[6:7], -1, 0
	v_cmp_lt_i32_e32 vcc, s2, v121
	s_waitcnt vmcnt(7)
	ds_write_b128 v196, v[44:47]
	s_waitcnt vmcnt(6)
	ds_write_b128 v196, v[48:51] offset:9216
	v_cndmask_b32_e64 v3, 0, 1, s[0:1]
	v_cndmask_b32_e64 v44, 0, 1, vcc
	v_cmp_lt_i32_e64 s[48:49], s2, v214
	s_and_b64 s[0:1], s[4:5], s[6:7]
	v_cndmask_b32_e64 v45, 0, 1, s[0:1]
	v_cndmask_b32_e64 v3, v44, v3, s[48:49]
	v_cndmask_b32_e64 v44, v44, v45, s[48:49]
	v_and_b32_e32 v3, 1, v3
	v_cmp_eq_u32_e64 s[52:53], 1, v3
	v_and_b32_e32 v3, 1, v44
	v_cmp_eq_u32_e64 s[50:51], 1, v3
	s_and_b64 s[0:1], s[52:53], s[50:51]
	s_andn2_b64 vcc, exec, s[0:1]
	s_mov_b64 s[0:1], -1
	s_cbranch_vccz .LBB0_651
	s_xor_b64 s[4:5], s[52:53], -1
	s_and_b64 vcc, exec, s[4:5]
	s_cbranch_vccz .LBB0_640
	v_mov_b64_e32 v[52:53], v[68:69]
	v_mov_b64_e32 v[56:57], v[76:77]
	v_mov_b64_e32 v[60:61], v[88:89]
	v_mov_b64_e32 v[64:65], v[108:109]
	s_andn2_b64 vcc, exec, s[50:51]
	v_mov_b64_e32 v[128:129], v[130:131]
	v_mov_b32_e32 v217, v219
	v_mov_b64_e32 v[54:55], v[70:71]
	v_mov_b64_e32 v[58:59], v[78:79]
	v_mov_b64_e32 v[62:63], v[90:91]
	v_mov_b64_e32 v[66:67], v[110:111]
	s_cbranch_vccnz .LBB0_639
	s_sub_i32 s2, s29, 32
	s_and_b64 s[0:1], s[48:49], exec
	s_cselect_b32 s0, s2, 0x1e0
	s_lshl_b32 s0, s0, 2
	v_cndmask_b32_e64 v3, 0, 1, s[48:49]
	s_add_i32 s0, s0, 0
	v_cmp_ne_u32_e64 s[50:51], 1, v3
	s_andn2_b64 vcc, exec, s[48:49]
	v_lshl_add_u32 v3, v159, 2, s0
	v_lshl_add_u32 v45, v160, 2, s0
	v_lshl_add_u32 v46, v161, 2, s0
	v_lshl_add_u32 v47, v162, 2, s0
	ds_read_b32 v48, v3 offset:36864
	ds_read_b32 v49, v45 offset:36864
	ds_read_b32 v50, v46 offset:36864
	ds_read_b32 v51, v47 offset:36864
.LBB0_632:
	s_and_b64 vcc, exec, s[50:51]
	v_lshl_add_u32 v3, v163, 2, s0
	v_lshl_add_u32 v45, v164, 2, s0
	v_lshl_add_u32 v46, v165, 2, s0
	v_lshl_add_u32 v47, v166, 2, s0
	ds_read_b32 v44, v3 offset:36864
	ds_read_b32 v45, v45 offset:36864
	ds_read_b32 v46, v46 offset:36864
	ds_read_b32 v47, v47 offset:36864

.LBB0_640:
	v_mov_b64_e32 v[72:73], v[92:93]
	v_mov_b64_e32 v[80:81], v[96:97]
	v_mov_b64_e32 v[84:85], v[104:105]
	v_mov_b64_e32 v[100:101], v[112:113]
	s_andn2_b64 vcc, exec, s[0:1]
	v_mov_b32_e32 v218, v220
	v_mov_b64_e32 v[74:75], v[94:95]
	v_mov_b64_e32 v[82:83], v[98:99]
	v_mov_b64_e32 v[86:87], v[106:107]
	v_mov_b64_e32 v[102:103], v[114:115]
	s_cbranch_vccnz .LBB0_650
	s_and_b64 s[0:1], s[48:49], exec
	s_cselect_b32 s0, s29, 0x1e0
	s_lshl_b32 s0, s0, 2
	v_cndmask_b32_e64 v3, 0, 1, s[48:49]
	s_add_i32 s0, s0, 0
	v_cmp_ne_u32_e64 s[50:51], 1, v3
	s_andn2_b64 vcc, exec, s[48:49]
	v_lshl_add_u32 v3, v159, 2, s0
	v_lshl_add_u32 v45, v160, 2, s0
	v_lshl_add_u32 v46, v161, 2, s0
	v_lshl_add_u32 v47, v162, 2, s0
	ds_read_b32 v48, v3 offset:36864
	ds_read_b32 v49, v45 offset:36864
	ds_read_b32 v50, v46 offset:36864
	ds_read_b32 v51, v47 offset:36864

.LBB0_651:
	s_andn2_b64 vcc, exec, s[0:1]
	s_cbranch_vccnz .LBB0_508
	s_and_b64 s[0:1], s[48:49], exec
	s_cselect_b32 s0, s29, 0x1e0
	s_lshl_b32 s0, s0, 2
	v_cndmask_b32_e64 v3, 0, 1, s[48:49]
	s_add_i32 s0, s0, 0
	v_cmp_ne_u32_e64 s[50:51], 1, v3
	s_andn2_b64 vcc, exec, s[48:49]
	v_lshl_add_u32 v3, v159, 2, s0
	v_lshl_add_u32 v45, v160, 2, s0
	v_lshl_add_u32 v46, v161, 2, s0
	v_lshl_add_u32 v47, v162, 2, s0
	ds_read_b32 v52, v3 offset:36864
	ds_read_b32 v53, v45 offset:36864
	ds_read_b32 v54, v46 offset:36864
	ds_read_b32 v55, v47 offset:36864

.LBB0_656:
	s_and_b64 vcc, exec, s[50:51]
	v_lshl_add_u32 v3, v167, 2, s0
	v_lshl_add_u32 v49, v168, 2, s0
	v_lshl_add_u32 v50, v169, 2, s0
	v_lshl_add_u32 v51, v170, 2, s0
	ds_read_b32 v60, v3 offset:36864
	ds_read_b32 v61, v49 offset:36864
	ds_read_b32 v62, v50 offset:36864
	ds_read_b32 v63, v51 offset:36864
.LBB0_658:
	s_and_b64 vcc, exec, s[50:51]
	v_lshl_add_u32 v3, v171, 2, s0
	v_lshl_add_u32 v49, v172, 2, s0
	v_lshl_add_u32 v50, v173, 2, s0
	v_lshl_add_u32 v51, v190, 2, s0
	ds_read_b32 v48, v3 offset:36864
	ds_read_b32 v49, v49 offset:36864
	ds_read_b32 v50, v50 offset:36864
	ds_read_b32 v51, v51 offset:36864
.LBB0_660:
	s_sub_i32 s2, s29, 32
	s_and_b64 s[0:1], s[48:49], exec
	s_cselect_b32 s0, s2, 0x1e0
	s_lshl_b32 s0, s0, 2
	s_add_i32 s0, s0, 0
	s_and_b64 vcc, exec, s[50:51]
	v_lshl_add_u32 v3, v159, 2, s0
	v_lshl_add_u32 v57, v160, 2, s0
	v_lshl_add_u32 v58, v161, 2, s0
	v_lshl_add_u32 v59, v162, 2, s0
	ds_read_b32 v56, v3 offset:36864
	ds_read_b32 v57, v57 offset:36864
	ds_read_b32 v58, v58 offset:36864
	ds_read_b32 v59, v59 offset:36864

.LBB0_664:
	s_and_b64 vcc, exec, s[50:51]
	v_lshl_add_u32 v3, v167, 2, s0
	v_lshl_add_u32 v72, v168, 2, s0
	v_lshl_add_u32 v73, v169, 2, s0
	v_lshl_add_u32 v74, v170, 2, s0
	ds_read_b32 v84, v3 offset:36864
	ds_read_b32 v85, v72 offset:36864
	ds_read_b32 v86, v73 offset:36864
	ds_read_b32 v87, v74 offset:36864
.LBB0_666:
	s_and_b64 vcc, exec, s[50:51]
	v_lshl_add_u32 v3, v171, 2, s0
	v_lshl_add_u32 v72, v172, 2, s0
	v_lshl_add_u32 v73, v173, 2, s0
	v_lshl_add_u32 v74, v190, 2, s0
	ds_read_b32 v100, v3 offset:36864
	ds_read_b32 v101, v72 offset:36864
	ds_read_b32 v102, v73 offset:36864
	ds_read_b32 v103, v74 offset:36864
	s_branch .LBB0_507
